# G=180: GEMM1 epilogues convert only 6 units (1536 W2 tiles), dedicated converters 9856 tiles
# baseline (speedup 1.0000x reference)
.LBB0_86:
	s_cmp_lt_i32 s50, 2
	s_cselect_b64 s[6:7], -1, 0
	s_and_b64 s[0:1], s[6:7], s[2:3]
	s_andn2_b64 vcc, exec, s[0:1]
	v_writelane_b32 v254, s60, 4
	s_cbranch_vccnz .LBB0_260
	s_mov_b64 s[2:3], s[80:81]
	s_load_dwordx2 s[8:9], s[2:3], 0xa8
	s_cmpk_lg_i32 s56, 0x100
	s_cselect_b32 s0, s56, 0xb4
	s_cmp_ge_i32 s78, s0
	s_mov_b64 s[4:5], -1
	s_cbranch_scc0 .LBB0_145
	s_sub_i32 s1, s78, s0
	s_cmpk_gt_i32 s1, 0x267f
	s_cbranch_scc1 .LBB0_144
	s_sub_i32 s20, s56, s0
	s_abs_i32 s4, s20
	v_cvt_f32_u32_e32 v1, s4
	s_load_dwordx2 s[10:11], s[2:3], 0x78
	s_load_dwordx2 s[12:13], s[2:3], 0x88
	s_sub_i32 s2, s20, s1
	s_add_i32 s3, s2, 0x267f
	v_rcp_iflag_f32_e32 v1, v1
	s_sub_i32 s2, 0xffffd981, s2
	s_xor_b32 s14, s3, s20
	s_sub_i32 s5, 0, s4
	v_mul_f32_e32 v1, 0x4f7ffffe, v1
	v_cvt_u32_f32_e32 v1, v1
	s_max_i32 s2, s3, s2
	s_ashr_i32 s3, s14, 31
	v_readfirstlane_b32 s14, v1
	s_mul_i32 s5, s5, s14
	s_mul_hi_u32 s5, s14, s5
	s_add_i32 s14, s14, s5
	s_mul_hi_u32 s5, s2, s14
	s_mul_i32 s14, s5, s4
	s_sub_i32 s2, s2, s14
	s_add_i32 s14, s5, 1
	s_sub_i32 s15, s2, s4
	s_cmp_ge_u32 s2, s4
	s_cselect_b32 s5, s14, s5
	s_cselect_b32 s2, s15, s2
	s_add_i32 s14, s5, 1
	s_cmp_ge_u32 s2, s4
	s_cselect_b32 s2, s14, s5
	s_xor_b32 s2, s2, s3
	s_sub_i32 s29, s2, s3
	s_lshl_b32 s21, s29, 2
	s_add_i32 s22, s21, -1
	s_cmp_gt_i32 s29, 0
	s_cselect_b64 s[2:3], -1, 0
	s_and_b64 s[4:5], s[2:3], exec
	s_cselect_b32 s18, 0, s22
	s_ashr_i32 s4, s18, 2
	s_mul_i32 s17, s4, s20
	s_add_i32 s17, s17, s1
	s_cmpk_gt_i32 s17, 0x1fff
	s_mov_b32 s5, 0
	s_cbranch_scc0 .LBB0_91
	s_add_i32 s4, s17, 0xffffe000
	s_lshr_b32 s4, s4, 7
	s_lshl_b64 s[4:5], s[4:5], 24
	s_waitcnt lgkmcnt(0)
	s_add_u32 s14, s12, s4
	s_addc_u32 s15, s13, s5
	s_lshl_b32 s4, s17, 4
	s_and_b32 s26, s4, 0x780
	s_lshl_b32 s4, s17, 8
	s_and_b32 s16, s4, 0x700
	s_mov_b64 s[4:5], 0x800
	s_cbranch_execz .LBB0_92
	s_branch .LBB0_93

.LBB0_367:
	s_lshr_b32 s0, s56, 31
	s_add_i32 s0, s56, s0
	s_ashr_i32 s0, s0, 1
	v_readlane_b32 s78, v254, 5
	s_cmp_ge_i32 s78, s0
	v_readlane_b32 s79, v254, 8
	v_readlane_b32 s60, v254, 4
	s_cbranch_scc0 .LBB0_409
	s_sub_i32 s10, s78, s0
	s_cmpk_gt_u32 s10, 0x37f
	s_waitcnt vmcnt(0) lgkmcnt(0)
	s_barrier
	s_cbranch_scc1 .LBB0_409
	s_sub_i32 s0, s56, s0
	s_abs_i32 s2, s0
	v_cvt_f32_u32_e32 v2, s2
	s_sub_i32 s3, s0, s10
	s_add_i32 s4, s3, 0x37f
	s_sub_i32 s3, 0xfffffc81, s3
	v_rcp_iflag_f32_e32 v2, v2
	s_xor_b32 s6, s4, s0
	s_sub_i32 s5, 0, s2
	s_max_i32 s3, s4, s3
	v_mul_f32_e32 v2, 0x4f7ffffe, v2
	v_cvt_u32_f32_e32 v2, v2
	s_ashr_i32 s4, s6, 31
	s_add_i32 s1, s10, 0x2680
	v_readfirstlane_b32 s6, v2
	s_mul_i32 s5, s5, s6
	s_mul_hi_u32 s5, s6, s5
	s_add_i32 s6, s6, s5
	s_mul_hi_u32 s5, s3, s6
	s_mul_i32 s6, s5, s2
	s_sub_i32 s3, s3, s6
	s_add_i32 s7, s5, 1
	s_sub_i32 s6, s3, s2
	s_cmp_ge_u32 s3, s2
	s_cselect_b32 s5, s7, s5
	s_cselect_b32 s3, s6, s3
	s_add_i32 s6, s5, 1
	s_cmp_ge_u32 s3, s2
	s_cselect_b32 s2, s6, s5
	s_xor_b32 s2, s2, s4
	s_sub_i32 s18, s2, s4
	s_lshl_b32 s12, s18, 2
	s_add_i32 s13, s12, -1
	s_cmp_gt_i32 s18, 0
	s_cselect_b64 s[2:3], -1, 0
	s_and_b64 s[4:5], s[2:3], exec
	s_cselect_b32 s11, 0, s13
	s_ashr_i32 s4, s11, 2
	s_mul_i32 s9, s4, s0
	s_add_i32 s9, s9, s1
	s_cmpk_gt_i32 s9, 0x1fff
	s_mov_b32 s5, 0
	s_cbranch_scc0 .LBB0_371
	s_add_i32 s4, s9, 0xffffe000
	s_lshr_b32 s4, s4, 7
	s_lshl_b64 s[4:5], s[4:5], 24
	v_readlane_b32 s34, v254, 13
	v_readlane_b32 s35, v254, 14
	s_add_u32 s6, s34, s4
	s_addc_u32 s7, s35, s5
	s_lshl_b32 s4, s9, 4
	s_and_b32 s19, s4, 0x780
	s_lshl_b32 s4, s9, 8
	v_readlane_b32 s30, v254, 11
	s_and_b32 s8, s4, 0x700
	v_readlane_b32 s31, v254, 12
	s_mov_b64 s[4:5], 0x800
	s_cbranch_execz .LBB0_372
	s_branch .LBB0_373

.LBB0_387:
	s_max_i32 s9, s12, 1
	s_add_u32 s18, s66, 0x5ee00000
	s_addc_u32 s19, s67, 0
	s_ashr_i32 s7, s6, 31
	s_lshl_b64 s[6:7], s[6:7], 2
	s_add_u32 s4, s4, s6
	v_add_u32_e32 v3, s8, v14
	v_mov_b32_e32 v11, 0
	s_addc_u32 s5, s5, s7
	v_mad_i64_i32 v[12:13], s[6:7], s2, v3, 0
	v_lshl_add_u64 v[12:13], v[12:13], 2, s[4:5]
	v_mov_b32_e32 v3, v11
	v_lshl_add_u64 v[12:13], v[12:13], 0, v[2:3]
	s_mov_b64 s[6:7], 0x300
	s_add_i32 s27, 0, 0x18000
	v_lshl_add_u64 v[12:13], v[12:13], 0, s[6:7]
	s_add_i32 m0, s27, s14
	v_add_u32_e32 v3, s8, v15
	global_load_lds_dwordx4 v[12:13], off nt
	v_mad_i64_i32 v[12:13], s[28:29], s2, v3, 0
	v_lshl_add_u64 v[12:13], v[12:13], 2, s[4:5]
	v_mov_b32_e32 v5, v11
	v_lshl_add_u64 v[12:13], v[12:13], 0, v[4:5]
	v_lshl_add_u64 v[12:13], v[12:13], 0, s[6:7]
	s_add_i32 m0, s27, s15
	v_add_u32_e32 v3, s8, v16
	global_load_lds_dwordx4 v[12:13], off nt
	v_mad_i64_i32 v[12:13], s[28:29], s2, v3, 0
	v_lshl_add_u64 v[12:13], v[12:13], 2, s[4:5]
	v_mov_b32_e32 v7, v11
	v_lshl_add_u64 v[12:13], v[12:13], 0, v[6:7]
	v_lshl_add_u64 v[12:13], v[12:13], 0, s[6:7]
	s_add_i32 m0, s27, s16
	v_add_u32_e32 v3, s8, v1
	global_load_lds_dwordx4 v[12:13], off nt
	v_mad_i64_i32 v[12:13], s[2:3], s2, v3, 0
	v_lshl_add_u64 v[12:13], v[12:13], 2, s[4:5]
	v_mov_b32_e32 v9, v11
	v_lshl_add_u64 v[12:13], v[12:13], 0, v[8:9]
	v_lshl_add_u64 v[12:13], v[12:13], 0, s[6:7]
	s_add_i32 m0, s27, s17
	v_lshrrev_b32_e32 v19, 3, v162
	global_load_lds_dwordx4 v[12:13], off nt
	v_readlane_b32 s2, v254, 15
	v_and_b32_e32 v3, 7, v0
	v_lshrrev_b32_e32 v9, 1, v162
	v_or_b32_e32 v17, s2, v19
	v_lshrrev_b32_e32 v7, 2, v17
	v_bitop3_b32 v7, v7, v0, 7 bitop3:0x78
	v_lshl_add_u32 v5, v3, 12, 0
	v_lshlrev_b32_e32 v7, 4, v7
	v_and_b32_e32 v9, 12, v9
	v_add3_u32 v18, v5, v7, v9
	ds_read2st64_b32 v[12:13], v18 offset1:1
	ds_read2st64_b32 v[20:21], v18 offset0:2 offset1:3
	ds_read2st64_b32 v[22:23], v18 offset0:4 offset1:5
	ds_read2st64_b32 v[24:25], v18 offset0:6 offset1:7
	v_lshlrev_b32_e32 v10, 4, v3
	s_lshl_b32 s2, s10, 15
	s_waitcnt lgkmcnt(0)
	v_mul_f32_e32 v7, 0x42000000, v20
	v_mul_f32_e32 v3, 0x42000000, v12
	v_mul_f32_e32 v5, 0x42000000, v13
	ds_read2st64_b32 v[12:13], v18 offset0:8 offset1:9
	v_mul_f32_e32 v9, 0x42000000, v21
	v_mul_f32_e32 v26, 0x42000000, v22
	v_mul_f32_e32 v27, 0x42000000, v23
	v_mul_f32_e32 v28, 0x42000000, v24
	v_mul_f32_e32 v29, 0x42000000, v25
	ds_read2st64_b32 v[20:21], v18 offset0:10 offset1:11
	ds_read2st64_b32 v[22:23], v18 offset0:12 offset1:13
	ds_read2st64_b32 v[24:25], v18 offset0:14 offset1:15
	s_add_i32 s2, s2, 0x3400000
	s_and_b32 s2, s2, 0x7c00000
	s_waitcnt lgkmcnt(0)
	v_mul_f32_e32 v30, 0x42000000, v12
	v_mul_f32_e32 v13, 0x42000000, v13
	v_mul_f32_e32 v31, 0x42000000, v20
	v_mul_f32_e32 v32, 0x42000000, v21
	v_mul_f32_e32 v33, 0x42000000, v22
	v_mul_f32_e32 v34, 0x42000000, v23
	v_mov_b32_e32 v20, v11
	v_mov_b32_e32 v21, v11
	v_mov_b32_e32 v22, v11
	v_mov_b32_e32 v23, v11
	s_add_u32 s4, s18, s2
	v_cvt_pk_fp8_f32 v20, v3, v5
	v_cvt_pk_fp8_f32 v21, v26, v27
	v_cvt_pk_fp8_f32 v22, v30, v13
	v_cvt_pk_fp8_f32 v23, v33, v34
	s_addc_u32 s5, s19, 0
	s_lshl_b32 s6, s1, 8
	s_and_b32 s6, s6, 0x700
	v_mul_f32_e32 v3, 0x42000000, v24
	v_mul_f32_e32 v5, 0x42000000, v25
	v_add_u32_e32 v12, s6, v17
	v_mov_b32_e32 v13, v11
	s_lshl_b32 s2, s1, 4
	v_cvt_pk_fp8_f32 v20, v7, v9 op_sel:[0,0,1]
	v_cvt_pk_fp8_f32 v21, v28, v29 op_sel:[0,0,1]
	v_cvt_pk_fp8_f32 v22, v31, v32 op_sel:[0,0,1]
	v_cvt_pk_fp8_f32 v23, v3, v5 op_sel:[0,0,1]
	v_lshlrev_b64 v[24:25], 11, v[12:13]
	s_mov_b32 s3, 0
	s_and_b32 s2, s2, 0x780
	v_lshl_add_u64 v[24:25], s[4:5], 0, v[24:25]
	v_lshl_add_u64 v[24:25], v[24:25], 0, s[2:3]
	v_lshl_add_u64 v[24:25], v[24:25], 0, v[10:11]
	s_cmp_eq_u32 s9, 1
	global_store_dwordx4 v[24:25], v[20:23], off nt
	s_cbranch_scc1 .LBB0_408
	s_min_i32 s27, s13, 4
	s_ashr_i32 s6, s27, 2
	s_waitcnt vmcnt(9)
	s_barrier
	s_mul_i32 s29, s6, s0
	s_add_i32 s29, s29, s1
	s_cmpk_lt_i32 s29, 0x2000
	s_cbranch_scc1 .LBB0_390
	s_add_i32 s6, s29, 0xffffe000
	s_lshr_b32 s6, s6, 7
	s_mov_b32 s7, 0
	s_lshl_b64 s[6:7], s[6:7], 24
	s_add_u32 s8, s34, s6
	s_addc_u32 s9, s35, s7
	s_lshl_b32 s6, s29, 4
	s_and_b32 s28, s6, 0x780
	s_lshl_b32 s6, s29, 8
	s_and_b32 s10, s6, 0x700
	s_mov_b64 s[6:7], 0
	s_branch .LBB0_391

.LBB0_730:
	v_readlane_b32 s92, v254, 5
	s_nop 3
	s_lshl_b32 s93, s80, 8
	s_add_u32 s92, s92, s93
	s_add_u32 s92, s92, 2560
	s_cmp_lt_u32 s92, 0x1000
	s_cselect_b32 s32, 1, 0
	s_cbranch_scc0 .Lp7c_skip1
	s_lshr_b32 s93, s92, 3
	s_lshl_b32 s93, s93, 20
	s_and_b32 s94, s92, 7
	s_lshl_b32 s95, s94, 10
	s_or_b32 s93, s93, s95
	s_lshl_b32 s95, s57, 7
	s_or_b32 s93, s93, s95
	s_add_u32 s90, s14, s93
	s_addc_u32 s91, s15, 0
	s_lshr_b32 s93, s92, 7
	s_lshl_b32 s93, s93, 22
	s_lshl_b32 s94, s94, 19
	s_or_b32 s93, s93, s94
	s_bfe_u32 s94, s92, 0x40003
	s_lshl_b32 s94, s94, 7
	s_or_b32 s93, s93, s94
	s_lshl_b32 s94, s57, 16
	s_or_b32 s93, s93, s94
	s_add_u32 s93, s93, 0x5ee00000
	s_add_u32 s88, s48, s93
	s_addc_u32 s89, s49, 0
	global_load_dwordx4 v[216:219], v249, s[90:91] nt
	s_add_u32 s90, s90, 0x2000
	s_addc_u32 s91, s91, 0
	global_load_dwordx4 v[220:223], v249, s[90:91] nt
	s_add_u32 s90, s90, 0x2000
	s_addc_u32 s91, s91, 0
	global_load_dwordx4 v[224:227], v249, s[90:91] nt
	s_add_u32 s90, s90, 0x2000
	s_addc_u32 s91, s91, 0
	global_load_dwordx4 v[228:231], v249, s[90:91] nt
	s_add_u32 s90, s90, 0x2000
	s_addc_u32 s91, s91, 0
	global_load_dwordx4 v[232:235], v249, s[90:91] nt
	s_add_u32 s90, s90, 0x2000
	s_addc_u32 s91, s91, 0
	global_load_dwordx4 v[236:239], v249, s[90:91] nt
	s_add_u32 s90, s90, 0x2000
	s_addc_u32 s91, s91, 0
	global_load_dwordx4 v[240:243], v249, s[90:91] nt
	s_add_u32 s90, s90, 0x2000
	s_addc_u32 s91, s91, 0
	global_load_dwordx4 v[244:247], v249, s[90:91] nt
	s_add_u32 s90, s90, 0x2000
	s_addc_u32 s91, s91, 0

.LBB0_741:
	s_or_b64 exec, exec, s[16:17]
	s_waitcnt lgkmcnt(0)
	s_barrier
	ds_read_b32 v6, v42
	s_mov_b64 s[16:17], -1
	s_waitcnt lgkmcnt(0)
	v_cmp_lt_i32_e32 vcc, s25, v6
	v_readfirstlane_b32 s4, v6
	s_cbranch_vccnz .LBB0_736
	s_add_i32 s18, s4, 0x2a00
	s_cmpk_gt_i32 s4, 0xf5ff
	s_cbranch_scc0 .LBB0_744
	s_addk_i32 s4, 0xa00
	s_lshr_b32 s4, s4, 7
	s_lshl_b64 s[16:17], s[4:5], 22
	s_lshl_b64 s[20:21], s[4:5], 24
	s_add_u32 s19, s14, s20
	s_addc_u32 s21, s15, s21
	s_add_u32 s16, s22, s16
	s_addc_u32 s17, s23, s17
	s_lshl_b32 s20, s18, 8
	s_lshl_b32 s4, s18, 4
	s_and_b32 s27, s20, 0x700
	s_and_b32 s26, s4, 0x7f0
	s_and_b32 s4, s4, 0x780
	s_lshl_b32 s20, s27, 2
	s_add_u32 s20, s19, s20
	s_addc_u32 s21, s21, 0
	v_or_b32_e32 v43, s4, v8
	v_lshl_add_u64 v[6:7], s[20:21], 0, v[2:3]
	v_lshlrev_b32_e32 v44, 13, v43
	v_mov_b32_e32 v45, v3
	v_or_b32_e32 v43, s4, v9
	v_lshl_add_u64 v[52:53], v[6:7], 0, v[44:45]
	v_lshlrev_b32_e32 v44, 13, v43
	v_or_b32_e32 v43, s4, v11
	v_lshl_add_u64 v[54:55], v[6:7], 0, v[44:45]
	global_load_dwordx4 v[44:47], v[52:53], off
	global_load_dwordx4 v[48:51], v[54:55], off
	v_lshlrev_b32_e32 v52, 13, v43
	v_mov_b32_e32 v53, v3
	v_or_b32_e32 v43, s4, v13
	v_lshl_add_u64 v[60:61], v[6:7], 0, v[52:53]
	v_lshlrev_b32_e32 v52, 13, v43
	v_or_b32_e32 v43, s4, v15
	v_lshl_add_u64 v[62:63], v[6:7], 0, v[52:53]
	global_load_dwordx4 v[52:55], v[60:61], off
	global_load_dwordx4 v[56:59], v[62:63], off
	v_lshlrev_b32_e32 v60, 13, v43
	v_mov_b32_e32 v61, v3
	v_or_b32_e32 v43, s4, v17
	v_lshl_add_u64 v[68:69], v[6:7], 0, v[60:61]
	v_lshlrev_b32_e32 v60, 13, v43
	v_or_b32_e32 v43, s4, v19
	v_lshl_add_u64 v[70:71], v[6:7], 0, v[60:61]
	global_load_dwordx4 v[60:63], v[68:69], off
	global_load_dwordx4 v[64:67], v[70:71], off
	v_lshlrev_b32_e32 v68, 13, v43
	v_mov_b32_e32 v69, v3
	v_or_b32_e32 v43, s4, v21
	v_lshl_add_u64 v[76:77], v[6:7], 0, v[68:69]
	v_lshlrev_b32_e32 v68, 13, v43
	v_or_b32_e32 v43, s4, v23
	v_lshl_add_u64 v[78:79], v[6:7], 0, v[68:69]
	global_load_dwordx4 v[68:71], v[76:77], off
	global_load_dwordx4 v[72:75], v[78:79], off
	v_lshlrev_b32_e32 v76, 13, v43
	v_mov_b32_e32 v77, v3
	v_or_b32_e32 v43, s4, v25
	v_lshl_add_u64 v[84:85], v[6:7], 0, v[76:77]
	v_lshlrev_b32_e32 v76, 13, v43
	v_or_b32_e32 v43, s4, v27
	v_lshl_add_u64 v[86:87], v[6:7], 0, v[76:77]
	global_load_dwordx4 v[76:79], v[84:85], off
	global_load_dwordx4 v[80:83], v[86:87], off
	v_lshlrev_b32_e32 v84, 13, v43
	v_mov_b32_e32 v85, v3
	v_or_b32_e32 v43, s4, v29
	v_lshl_add_u64 v[92:93], v[6:7], 0, v[84:85]
	v_lshlrev_b32_e32 v84, 13, v43
	v_or_b32_e32 v43, s4, v31
	v_lshl_add_u64 v[94:95], v[6:7], 0, v[84:85]
	global_load_dwordx4 v[84:87], v[92:93], off
	global_load_dwordx4 v[88:91], v[94:95], off
	v_lshlrev_b32_e32 v92, 13, v43
	v_mov_b32_e32 v93, v3
	v_or_b32_e32 v43, s4, v33
	v_lshl_add_u64 v[100:101], v[6:7], 0, v[92:93]
	v_lshlrev_b32_e32 v92, 13, v43
	v_or_b32_e32 v43, s26, v35
	v_lshl_add_u64 v[102:103], v[6:7], 0, v[92:93]
	global_load_dwordx4 v[92:95], v[100:101], off
	global_load_dwordx4 v[96:99], v[102:103], off
	v_lshlrev_b32_e32 v100, 13, v43
	v_mov_b32_e32 v101, v3
	v_or_b32_e32 v43, s4, v37
	v_lshl_add_u64 v[108:109], v[6:7], 0, v[100:101]
	v_lshlrev_b32_e32 v100, 13, v43
	v_lshl_add_u64 v[6:7], v[6:7], 0, v[100:101]
	global_load_dwordx4 v[100:103], v[108:109], off
	global_load_dwordx4 v[104:107], v[6:7], off
	v_or_b32_e32 v6, s27, v39
	v_lshlrev_b32_e32 v6, 11, v6
	v_mov_b32_e32 v7, v3
	v_lshl_add_u64 v[6:7], s[16:17], 0, v[6:7]
	v_lshl_add_u64 v[6:7], v[6:7], 0, s[4:5]
	v_lshl_add_u64 v[6:7], v[6:7], 0, v[4:5]
	s_mov_b64 s[16:17], 0
	s_waitcnt vmcnt(15)
	ds_write_b128 v1, v[44:47]
	s_waitcnt vmcnt(14)
	ds_write_b128 v10, v[48:51]
	s_waitcnt vmcnt(13)
	ds_write_b128 v12, v[52:55]
	s_waitcnt vmcnt(12)
	ds_write_b128 v14, v[56:59]
	s_waitcnt vmcnt(11)
	ds_write_b128 v16, v[60:63]
	s_waitcnt vmcnt(10)
	ds_write_b128 v18, v[64:67]
	s_waitcnt vmcnt(9)
	ds_write_b128 v20, v[68:71]
	s_waitcnt vmcnt(8)
	ds_write_b128 v22, v[72:75]
	s_waitcnt vmcnt(7)
	ds_write_b128 v24, v[76:79] offset:64
	s_waitcnt vmcnt(6)
	ds_write_b128 v26, v[80:83] offset:64
	s_waitcnt vmcnt(5)
	ds_write_b128 v28, v[84:87] offset:64
	s_waitcnt vmcnt(4)
	ds_write_b128 v30, v[88:91] offset:64
	s_waitcnt vmcnt(3)
	ds_write_b128 v32, v[92:95] offset:64
	s_waitcnt vmcnt(2)
	ds_write_b128 v34, v[96:99] offset:64
	s_waitcnt vmcnt(1)
	ds_write_b128 v36, v[100:103] offset:64
	s_waitcnt vmcnt(0)
	ds_write_b128 v38, v[104:107]
	s_waitcnt lgkmcnt(0)
	s_barrier
	ds_read_b32 v43, v40
	ds_read_b32 v44, v40 offset:1040
	ds_read_b32 v45, v40 offset:2080
	ds_read_b32 v46, v40 offset:3120
	ds_read_b32 v47, v40 offset:4160
	ds_read_b32 v48, v40 offset:5200
	ds_read_b32 v49, v40 offset:6240
	ds_read_b32 v50, v40 offset:7280
	s_waitcnt lgkmcnt(6)
	v_mul_f32_e32 v51, 0x42000000, v44
	s_waitcnt lgkmcnt(5)
	v_mul_f32_e32 v52, 0x42000000, v45
	s_waitcnt lgkmcnt(4)
	v_mul_f32_e32 v53, 0x42000000, v46
	s_waitcnt lgkmcnt(3)
	v_mul_f32_e32 v46, 0x42000000, v47
	s_waitcnt lgkmcnt(2)
	v_mul_f32_e32 v47, 0x42000000, v48
	s_waitcnt lgkmcnt(1)
	v_mul_f32_e32 v48, 0x42000000, v49
	s_waitcnt lgkmcnt(0)
	v_mul_f32_e32 v49, 0x42000000, v50
	ds_read_b32 v44, v40 offset:8320
	ds_read_b32 v45, v40 offset:9360
	ds_read_b32 v50, v40 offset:10400
	ds_read_b32 v54, v40 offset:11440
	ds_read_b32 v55, v40 offset:12480
	ds_read_b32 v56, v40 offset:13520
	ds_read_b32 v57, v40 offset:14560
	ds_read_b32 v58, v40 offset:15600
	s_waitcnt lgkmcnt(6)
	v_mul_f32_e32 v60, 0x42000000, v45
	v_mov_b32_e32 v45, v3
	v_mul_f32_e32 v43, 0x42000000, v43
	v_mul_f32_e32 v59, 0x42000000, v44
	v_mov_b32_e32 v44, v3
	v_cvt_pk_fp8_f32 v45, v46, v47
	v_mov_b32_e32 v46, v3
	v_cvt_pk_fp8_f32 v44, v43, v51
	v_cvt_pk_fp8_f32 v46, v59, v60
	s_waitcnt lgkmcnt(5)
	v_mul_f32_e32 v50, 0x42000000, v50
	s_waitcnt lgkmcnt(4)
	v_mul_f32_e32 v54, 0x42000000, v54
	s_waitcnt lgkmcnt(3)
	v_mul_f32_e32 v55, 0x42000000, v55
	s_waitcnt lgkmcnt(2)
	v_mul_f32_e32 v56, 0x42000000, v56
	v_mov_b32_e32 v47, v3
	v_cvt_pk_fp8_f32 v44, v52, v53 op_sel:[0,0,1]
	v_cvt_pk_fp8_f32 v45, v48, v49 op_sel:[0,0,1]
	v_cvt_pk_fp8_f32 v46, v50, v54 op_sel:[0,0,1]
	ds_read_b32 v43, v40 offset:16640
	ds_read_b32 v48, v40 offset:17680
	ds_read_b32 v49, v40 offset:18720
	ds_read_b32 v50, v40 offset:19760
	ds_read_b32 v51, v40 offset:20800
	ds_read_b32 v52, v40 offset:21840
	ds_read_b32 v53, v40 offset:22880
	ds_read_b32 v54, v40 offset:23920
	v_cvt_pk_fp8_f32 v47, v55, v56
	s_waitcnt lgkmcnt(9)
	v_mul_f32_e32 v57, 0x42000000, v57
	s_waitcnt lgkmcnt(8)
	v_mul_f32_e32 v58, 0x42000000, v58
	s_waitcnt lgkmcnt(6)
	v_mul_f32_e32 v55, 0x42000000, v48
	v_cvt_pk_fp8_f32 v47, v57, v58 op_sel:[0,0,1]
	s_waitcnt lgkmcnt(5)
	v_mul_f32_e32 v56, 0x42000000, v49
	s_waitcnt lgkmcnt(4)
	v_mul_f32_e32 v57, 0x42000000, v50
	s_waitcnt lgkmcnt(3)
	v_mul_f32_e32 v50, 0x42000000, v51
	s_waitcnt lgkmcnt(2)
	v_mul_f32_e32 v51, 0x42000000, v52
	s_waitcnt lgkmcnt(1)
	v_mul_f32_e32 v52, 0x42000000, v53
	s_waitcnt lgkmcnt(0)
	v_mul_f32_e32 v53, 0x42000000, v54
	ds_read_b32 v48, v40 offset:24960
	ds_read_b32 v49, v40 offset:26000
	ds_read_b32 v54, v40 offset:27040
	ds_read_b32 v58, v40 offset:28080
	ds_read_b32 v59, v40 offset:29120
	ds_read_b32 v60, v40 offset:30160
	ds_read_b32 v61, v40 offset:31200
	ds_read_b32 v62, v40 offset:32240
	s_waitcnt lgkmcnt(6)
	v_mul_f32_e32 v64, 0x42000000, v49
	v_mov_b32_e32 v49, v3
	v_mul_f32_e32 v43, 0x42000000, v43
	v_mul_f32_e32 v63, 0x42000000, v48
	v_mov_b32_e32 v48, v3
	v_cvt_pk_fp8_f32 v49, v50, v51
	v_mov_b32_e32 v50, v3
	v_cvt_pk_fp8_f32 v48, v43, v55
	v_cvt_pk_fp8_f32 v50, v63, v64
	s_waitcnt lgkmcnt(5)
	v_mul_f32_e32 v54, 0x42000000, v54
	s_waitcnt lgkmcnt(4)
	v_mul_f32_e32 v58, 0x42000000, v58
	s_waitcnt lgkmcnt(3)
	v_mul_f32_e32 v59, 0x42000000, v59
	s_waitcnt lgkmcnt(2)
	v_mul_f32_e32 v60, 0x42000000, v60
	v_mov_b32_e32 v51, v3
	v_cvt_pk_fp8_f32 v48, v56, v57 op_sel:[0,0,1]
	v_cvt_pk_fp8_f32 v49, v52, v53 op_sel:[0,0,1]
	v_cvt_pk_fp8_f32 v50, v54, v58 op_sel:[0,0,1]
	ds_read_b32 v43, v40 offset:33280
	ds_read_b32 v52, v40 offset:34320
	ds_read_b32 v53, v40 offset:35360
	ds_read_b32 v54, v40 offset:36400
	ds_read_b32 v55, v40 offset:37440
	ds_read_b32 v56, v40 offset:38480
	ds_read_b32 v57, v40 offset:39520
	ds_read_b32 v58, v40 offset:40560
	v_cvt_pk_fp8_f32 v51, v59, v60
	s_waitcnt lgkmcnt(9)
	v_mul_f32_e32 v61, 0x42000000, v61
	s_waitcnt lgkmcnt(8)
	v_mul_f32_e32 v62, 0x42000000, v62
	s_waitcnt lgkmcnt(6)
	v_mul_f32_e32 v59, 0x42000000, v52
	v_cvt_pk_fp8_f32 v51, v61, v62 op_sel:[0,0,1]
	s_waitcnt lgkmcnt(5)
	v_mul_f32_e32 v60, 0x42000000, v53
	s_waitcnt lgkmcnt(4)
	v_mul_f32_e32 v61, 0x42000000, v54
	s_waitcnt lgkmcnt(3)
	v_mul_f32_e32 v54, 0x42000000, v55
	s_waitcnt lgkmcnt(2)
	v_mul_f32_e32 v55, 0x42000000, v56
	s_waitcnt lgkmcnt(1)
	v_mul_f32_e32 v56, 0x42000000, v57
	s_waitcnt lgkmcnt(0)
	v_mul_f32_e32 v57, 0x42000000, v58
	ds_read_b32 v52, v40 offset:41600
	ds_read_b32 v53, v40 offset:42640
	ds_read_b32 v58, v40 offset:43680
	ds_read_b32 v62, v40 offset:44720
	ds_read_b32 v63, v40 offset:45760
	ds_read_b32 v64, v40 offset:46800
	ds_read_b32 v65, v40 offset:47840
	ds_read_b32 v66, v40 offset:48880
	s_waitcnt lgkmcnt(6)
	v_mul_f32_e32 v68, 0x42000000, v53
	v_mov_b32_e32 v53, v3
	v_mul_f32_e32 v43, 0x42000000, v43
	v_mul_f32_e32 v67, 0x42000000, v52
	v_mov_b32_e32 v52, v3
	v_cvt_pk_fp8_f32 v53, v54, v55
	v_mov_b32_e32 v54, v3
	v_cvt_pk_fp8_f32 v52, v43, v59
	v_cvt_pk_fp8_f32 v54, v67, v68
	s_waitcnt lgkmcnt(5)
	v_mul_f32_e32 v58, 0x42000000, v58
	s_waitcnt lgkmcnt(4)
	v_mul_f32_e32 v62, 0x42000000, v62
	s_waitcnt lgkmcnt(3)
	v_mul_f32_e32 v63, 0x42000000, v63
	s_waitcnt lgkmcnt(2)
	v_mul_f32_e32 v64, 0x42000000, v64
	v_mov_b32_e32 v55, v3
	v_cvt_pk_fp8_f32 v52, v60, v61 op_sel:[0,0,1]
	v_cvt_pk_fp8_f32 v53, v56, v57 op_sel:[0,0,1]
	v_cvt_pk_fp8_f32 v54, v58, v62 op_sel:[0,0,1]
	ds_read_b32 v43, v40 offset:49920
	ds_read_b32 v56, v40 offset:50960
	ds_read_b32 v57, v40 offset:52000
	ds_read_b32 v58, v40 offset:53040
	ds_read_b32 v59, v40 offset:54080
	ds_read_b32 v60, v40 offset:55120
	ds_read_b32 v61, v40 offset:56160
	ds_read_b32 v62, v40 offset:57200
	v_cvt_pk_fp8_f32 v55, v63, v64
	s_waitcnt lgkmcnt(9)
	v_mul_f32_e32 v65, 0x42000000, v65
	s_waitcnt lgkmcnt(8)
	v_mul_f32_e32 v66, 0x42000000, v66
	s_waitcnt lgkmcnt(6)
	v_mul_f32_e32 v63, 0x42000000, v56
	v_cvt_pk_fp8_f32 v55, v65, v66 op_sel:[0,0,1]
	s_waitcnt lgkmcnt(5)
	v_mul_f32_e32 v64, 0x42000000, v57
	s_waitcnt lgkmcnt(4)
	v_mul_f32_e32 v65, 0x42000000, v58
	s_waitcnt lgkmcnt(3)
	v_mul_f32_e32 v58, 0x42000000, v59
	s_waitcnt lgkmcnt(2)
	v_mul_f32_e32 v59, 0x42000000, v60
	s_waitcnt lgkmcnt(1)
	v_mul_f32_e32 v60, 0x42000000, v61
	s_waitcnt lgkmcnt(0)
	v_mul_f32_e32 v61, 0x42000000, v62
	ds_read_b32 v56, v40 offset:58240
	ds_read_b32 v57, v40 offset:59280
	ds_read_b32 v62, v40 offset:60320
	ds_read_b32 v66, v40 offset:61360
	ds_read_b32 v67, v40 offset:62400
	ds_read_b32 v68, v40 offset:63440
	ds_read_b32 v69, v40 offset:64480
	ds_read_b32 v70, v40 offset:65520
	s_waitcnt lgkmcnt(6)
	v_mul_f32_e32 v72, 0x42000000, v57
	v_mov_b32_e32 v57, v3
	v_mul_f32_e32 v43, 0x42000000, v43
	v_mul_f32_e32 v71, 0x42000000, v56
	s_waitcnt lgkmcnt(3)
	v_mul_f32_e32 v67, 0x42000000, v67
	s_waitcnt lgkmcnt(2)
	v_mul_f32_e32 v68, 0x42000000, v68
	v_mov_b32_e32 v56, v3
	v_cvt_pk_fp8_f32 v57, v58, v59
	v_mov_b32_e32 v58, v3
	v_mov_b32_e32 v59, v3
	v_cvt_pk_fp8_f32 v56, v43, v63
	v_cvt_pk_fp8_f32 v58, v71, v72
	v_cvt_pk_fp8_f32 v59, v67, v68
	v_mul_f32_e32 v62, 0x42000000, v62
	v_mul_f32_e32 v66, 0x42000000, v66
	s_waitcnt lgkmcnt(1)
	v_mul_f32_e32 v69, 0x42000000, v69
	s_waitcnt lgkmcnt(0)
	v_mul_f32_e32 v70, 0x42000000, v70
	v_cvt_pk_fp8_f32 v56, v64, v65 op_sel:[0,0,1]
	v_cvt_pk_fp8_f32 v57, v60, v61 op_sel:[0,0,1]
	v_cvt_pk_fp8_f32 v58, v62, v66 op_sel:[0,0,1]
	v_cvt_pk_fp8_f32 v59, v69, v70 op_sel:[0,0,1]
	global_store_dwordx4 v[6:7], v[44:47], off
	global_store_dwordx4 v[6:7], v[48:51], off offset:16
	global_store_dwordx4 v[6:7], v[52:55], off offset:32
	global_store_dwordx4 v[6:7], v[56:59], off offset:48
	s_waitcnt lgkmcnt(0)
	s_barrier
